# E36: E25 + instruction selection (lever 7) in the NSA sel-far softmax: the 32 per-element v_fmamk/v_fmac scale-and-shift ops become 16 in-place v_pk_fma_f32 (bit-identical fused ops)
# baseline (speedup 1.0000x reference)
.LBB0_697:
	s_mov_b32 s100, 0x3fb8aa3b
	v_sub_f32_e32 v0, v5, v134
	v_pk_fma_f32 v[98:99], v[98:99], s[100:101], v[0:1] op_sel_hi:[1,0,0]
	v_pk_fma_f32 v[100:101], v[100:101], s[100:101], v[0:1] op_sel_hi:[1,0,0]
	v_pk_fma_f32 v[94:95], v[94:95], s[100:101], v[0:1] op_sel_hi:[1,0,0]
	v_pk_fma_f32 v[96:97], v[96:97], s[100:101], v[0:1] op_sel_hi:[1,0,0]
	v_pk_fma_f32 v[90:91], v[90:91], s[100:101], v[0:1] op_sel_hi:[1,0,0]
	v_pk_fma_f32 v[92:93], v[92:93], s[100:101], v[0:1] op_sel_hi:[1,0,0]
	v_pk_fma_f32 v[86:87], v[86:87], s[100:101], v[0:1] op_sel_hi:[1,0,0]
	v_pk_fma_f32 v[88:89], v[88:89], s[100:101], v[0:1] op_sel_hi:[1,0,0]
	v_exp_f32_e32 v98, v98
	v_exp_f32_e32 v99, v99
	v_exp_f32_e32 v100, v100
	v_exp_f32_e32 v101, v101
	v_exp_f32_e32 v94, v94
	v_add_f32_e32 v5, 0, v98
	v_exp_f32_e32 v95, v95
	v_add_f32_e32 v5, v99, v5
	v_exp_f32_e32 v96, v96
	v_add_f32_e32 v5, v100, v5
	v_exp_f32_e32 v97, v97
	v_add_f32_e32 v5, v101, v5
	v_exp_f32_e32 v90, v90
	v_add_f32_e32 v5, v94, v5
	v_exp_f32_e32 v91, v91
	v_add_f32_e32 v5, v95, v5
	v_exp_f32_e32 v92, v92
	v_add_f32_e32 v5, v96, v5
	v_exp_f32_e32 v93, v93
	v_add_f32_e32 v5, v97, v5
	v_exp_f32_e32 v198, v86
	v_add_f32_e32 v5, v90, v5
	v_exp_f32_e32 v199, v87
	v_add_f32_e32 v5, v91, v5
	v_exp_f32_e32 v200, v88
	v_add_f32_e32 v5, v92, v5
	v_exp_f32_e32 v0, v89
	v_add_f32_e32 v5, v93, v5
	v_add_f32_e32 v5, v198, v5
	v_add_f32_e32 v5, v199, v5
	v_add_f32_e32 v5, v200, v5
	v_add_f32_e32 v5, v0, v5
	v_fmac_f32_e32 v5, v136, v4
	v_sub_f32_e32 v4, v137, v125
	v_pk_fma_f32 v[82:83], v[82:83], s[100:101], v[4:5] op_sel_hi:[1,0,0]
	v_pk_fma_f32 v[84:85], v[84:85], s[100:101], v[4:5] op_sel_hi:[1,0,0]
	v_pk_fma_f32 v[78:79], v[78:79], s[100:101], v[4:5] op_sel_hi:[1,0,0]
	v_pk_fma_f32 v[80:81], v[80:81], s[100:101], v[4:5] op_sel_hi:[1,0,0]
	v_pk_fma_f32 v[74:75], v[74:75], s[100:101], v[4:5] op_sel_hi:[1,0,0]
	v_pk_fma_f32 v[76:77], v[76:77], s[100:101], v[4:5] op_sel_hi:[1,0,0]
	v_pk_fma_f32 v[70:71], v[70:71], s[100:101], v[4:5] op_sel_hi:[1,0,0]
	v_pk_fma_f32 v[72:73], v[72:73], s[100:101], v[4:5] op_sel_hi:[1,0,0]
	v_exp_f32_e32 v82, v82
	v_exp_f32_e32 v83, v83
	v_exp_f32_e32 v84, v84
	v_exp_f32_e32 v85, v85
	v_exp_f32_e32 v87, v78
	v_add_f32_e32 v86, 0, v82
	v_exp_f32_e32 v88, v79
	v_add_f32_e32 v86, v83, v86
	v_exp_f32_e32 v89, v80
	v_add_f32_e32 v86, v84, v86
	v_exp_f32_e32 v81, v81
	v_add_f32_e32 v86, v85, v86
	v_exp_f32_e32 v136, v74
	v_add_f32_e32 v78, v87, v86
	v_exp_f32_e32 v137, v75
	v_add_f32_e32 v78, v88, v78
	v_exp_f32_e32 v201, v76
	v_add_f32_e32 v78, v89, v78
	v_exp_f32_e32 v202, v77
	v_add_f32_e32 v78, v81, v78
	v_exp_f32_e32 v203, v70
	v_add_f32_e32 v74, v136, v78
	v_exp_f32_e32 v204, v71
	v_add_f32_e32 v74, v137, v74
	v_exp_f32_e32 v205, v72
	v_add_f32_e32 v74, v201, v74
	v_exp_f32_e32 v4, v73
	v_add_f32_e32 v74, v202, v74
	v_add_f32_e32 v70, v203, v74
	v_add_f32_e32 v70, v204, v70
	v_add_f32_e32 v70, v205, v70
	v_add_f32_e32 v133, v4, v70
	s_cmp_eq_u32 s83, 0
	s_cselect_b32 s0, 0x8000, s79
	s_add_i32 s0, s0, 0
	v_fmac_f32_e32 v133, v135, v2
	v_add_u32_e32 v2, s0, v142
	ds_read_b128 v[70:73], v2
	ds_read_b128 v[74:77], v2 offset:2048
	v_cvt_pk_bf16_f32 v78, v82, v83
	v_cvt_pk_bf16_f32 v79, v84, v85
	ds_read_b128 v[82:85], v2 offset:4096
	v_cvt_pk_bf16_f32 v80, v87, v88
	v_cvt_pk_bf16_f32 v81, v89, v81
	v_cvt_pk_bf16_f32 v86, v98, v99
	v_cvt_pk_bf16_f32 v87, v100, v101
	v_cvt_pk_bf16_f32 v88, v94, v95
	v_cvt_pk_bf16_f32 v89, v96, v97
	s_waitcnt lgkmcnt(2)
	v_mfma_f32_16x16x32_bf16 v[66:69], v[70:73], v[78:81], v[66:69]
	v_mfma_f32_16x16x32_bf16 v[34:37], v[70:73], v[86:89], v[34:37]
	ds_read_b128 v[70:73], v2 offset:6144
	s_waitcnt lgkmcnt(2)
	v_mfma_f32_16x16x32_bf16 v[62:65], v[74:77], v[78:81], v[62:65]
	v_mfma_f32_16x16x32_bf16 v[30:33], v[74:77], v[86:89], v[30:33]
	ds_read_b128 v[74:77], v2 offset:8192
	s_waitcnt lgkmcnt(2)
	v_mfma_f32_16x16x32_bf16 v[58:61], v[82:85], v[78:81], v[58:61]
	v_mfma_f32_16x16x32_bf16 v[26:29], v[82:85], v[86:89], v[26:29]
	ds_read_b128 v[82:85], v2 offset:10240
	s_waitcnt lgkmcnt(2)
	v_mfma_f32_16x16x32_bf16 v[54:57], v[70:73], v[78:81], v[54:57]
	v_mfma_f32_16x16x32_bf16 v[22:25], v[70:73], v[86:89], v[22:25]
	ds_read_b128 v[70:73], v2 offset:12288
	s_waitcnt lgkmcnt(2)
	v_mfma_f32_16x16x32_bf16 v[50:53], v[74:77], v[78:81], v[50:53]
	v_mfma_f32_16x16x32_bf16 v[18:21], v[74:77], v[86:89], v[18:21]
	ds_read_b128 v[74:77], v2 offset:14336
	v_add_u32_e32 v2, s0, v146
	s_waitcnt lgkmcnt(2)
	v_mfma_f32_16x16x32_bf16 v[46:49], v[82:85], v[78:81], v[46:49]
	v_mfma_f32_16x16x32_bf16 v[14:17], v[82:85], v[86:89], v[14:17]
	ds_read_b128 v[82:85], v2
	s_waitcnt lgkmcnt(2)
	v_mfma_f32_16x16x32_bf16 v[42:45], v[70:73], v[78:81], v[42:45]
	v_mfma_f32_16x16x32_bf16 v[10:13], v[70:73], v[86:89], v[10:13]
	ds_read_b128 v[70:73], v2 offset:2048
	s_waitcnt lgkmcnt(2)
	v_mfma_f32_16x16x32_bf16 v[38:41], v[74:77], v[78:81], v[38:41]
	v_cvt_pk_bf16_f32 v78, v90, v91
	v_cvt_pk_bf16_f32 v79, v92, v93
	v_cvt_pk_bf16_f32 v80, v198, v199
	v_mfma_f32_16x16x32_bf16 v[6:9], v[74:77], v[86:89], v[6:9]
	ds_read_b128 v[86:89], v2 offset:4096
	v_cvt_pk_bf16_f32 v74, v136, v137
	v_cvt_pk_bf16_f32 v75, v201, v202
	v_cvt_pk_bf16_f32 v76, v203, v204
	v_cvt_pk_bf16_f32 v77, v205, v4
	v_cvt_pk_bf16_f32 v81, v200, v0
	s_nop 0
	s_waitcnt lgkmcnt(2)
	v_mfma_f32_16x16x32_bf16 v[66:69], v[82:85], v[74:77], v[66:69]
	v_mfma_f32_16x16x32_bf16 v[34:37], v[82:85], v[78:81], v[34:37]
	ds_read_b128 v[82:85], v2 offset:6144
	s_waitcnt lgkmcnt(2)
	v_mfma_f32_16x16x32_bf16 v[62:65], v[70:73], v[74:77], v[62:65]
	v_mfma_f32_16x16x32_bf16 v[30:33], v[70:73], v[78:81], v[30:33]
	ds_read_b128 v[70:73], v2 offset:8192
	s_waitcnt lgkmcnt(2)
	v_mfma_f32_16x16x32_bf16 v[58:61], v[86:89], v[74:77], v[58:61]
	v_mfma_f32_16x16x32_bf16 v[26:29], v[86:89], v[78:81], v[26:29]
	ds_read_b128 v[86:89], v2 offset:10240
	s_waitcnt lgkmcnt(2)
	v_mfma_f32_16x16x32_bf16 v[54:57], v[82:85], v[74:77], v[54:57]
	v_mfma_f32_16x16x32_bf16 v[22:25], v[82:85], v[78:81], v[22:25]
	ds_read_b128 v[82:85], v2 offset:12288
	s_waitcnt lgkmcnt(2)
	v_mfma_f32_16x16x32_bf16 v[50:53], v[70:73], v[74:77], v[50:53]
	v_mfma_f32_16x16x32_bf16 v[18:21], v[70:73], v[78:81], v[18:21]
	ds_read_b128 v[70:73], v2 offset:14336
	s_waitcnt lgkmcnt(2)
	v_mfma_f32_16x16x32_bf16 v[46:49], v[86:89], v[74:77], v[46:49]
	v_mfma_f32_16x16x32_bf16 v[14:17], v[86:89], v[78:81], v[14:17]
	s_waitcnt lgkmcnt(1)
	v_mfma_f32_16x16x32_bf16 v[42:45], v[82:85], v[74:77], v[42:45]
	v_mfma_f32_16x16x32_bf16 v[10:13], v[82:85], v[78:81], v[10:13]
	s_waitcnt lgkmcnt(0)
	v_mfma_f32_16x16x32_bf16 v[38:41], v[70:73], v[74:77], v[38:41]
	s_waitcnt vmcnt(0)
	s_add_i32 s33, s33, 1
	s_add_i32 s0, s8, s33
	v_mfma_f32_16x16x32_bf16 v[6:9], v[70:73], v[78:81], v[6:9]
	s_cmp_eq_u32 s0, 1
	s_cbranch_scc1 .Lx687_exit
	v_mov_b32_e32 v136, v5
	v_mov_b32_e32 v135, v133
	v_mov_b32_e32 v133, v125
	v_mov_b32_e32 v4, v134
	s_add_i32 s0, s33, -1
	s_and_b32 s83, s0, 1
	s_add_i32 s3, s3, 1
	s_lshl_b32 s0, s83, 14
	s_add_i32 s0, s0, 0
	v_add_u32_e32 v0, s0, v140
	s_add_i32 s1, s37, s33
	s_add_i32 s1, s1, -1
	s_mov_b32 s32, 0
	s_add_i32 s98, s33, -1
	s_cmp_ge_u32 s98, s86
	s_cbranch_scc1 .Lx687_pd
	s_cmp_ge_i32 s33, s42
	s_mov_b64 s[98:99], -1
	s_cbranch_scc0 .Lx687_a
	s_add_i32 s98, s8, s33
	s_cmp_ge_i32 s98, s43
	s_cselect_b32 s99, s82, 0
	s_add_i32 s22, s98, s99
	s_mov_b64 s[98:99], 0

.LBB0_700:
	s_lshl_b32 s8, s36, 19
	s_cmp_gt_i32 s82, s86
	s_cbranch_scc1 .LBB0_781
	s_sub_i32 s36, s2, s43
	s_sub_i32 s84, 0, s42
	s_cmp_ge_i32 s82, s42
	s_mov_b64 s[0:1], -1
	s_cbranch_scc0 .LBB0_704
	s_branch .LBB0_703
	s_nop 0
	s_nop 0
	s_nop 0
	s_nop 0
	s_nop 0
	s_nop 0
	s_nop 0
	s_nop 0
	s_nop 0
	s_nop 0
	s_nop 0
	s_nop 0
	s_nop 0
	s_nop 0
	s_nop 0
	s_nop 0
	s_nop 0
	s_nop 0
	s_nop 0
	s_nop 0
	s_nop 0
	s_nop 0
	s_nop 0
	s_nop 0
	s_nop 0
	s_nop 0
	s_nop 0
	s_nop 0
	s_nop 0
	s_nop 0
	s_nop 0
	s_nop 0
	s_nop 0
	s_nop 0
	s_nop 0
	s_nop 0
	s_nop 0
	s_nop 0
	s_nop 0
	s_nop 0
	s_nop 0
	s_nop 0
	s_nop 0
	s_nop 0
	s_nop 0
	s_nop 0
	s_nop 0
	s_nop 0
